# nt hint on the read-once f32 weight loads of the bf16/fp8 conversions (keeps intermediates in cache)
# speedup vs baseline: 1.0651x; 1.0074x over previous
.LBB0_12:
	v_add_u32_e32 v4, s4, v3
	v_mad_i64_i32 v[26:27], s[10:11], s14, v4, 0
	v_lshl_add_u64 v[26:27], v[26:27], 2, s[8:9]
	v_cndmask_b32_e64 v4, 0, v2, s[6:7]
	v_lshl_add_u64 v[26:27], s[12:13], 2, v[26:27]
	v_lshlrev_b32_e32 v4, 2, v4
	v_lshl_add_u64 v[26:27], v[26:27], 0, v[4:5]
	s_lshl_b32 s0, s14, 3
	v_lshl_add_u64 v[28:29], v[26:27], 0, s[0:1]
	v_lshl_add_u64 v[30:31], v[28:29], 0, s[0:1]
	v_lshl_add_u64 v[32:33], v[30:31], 0, s[0:1]
	v_lshl_add_u64 v[34:35], v[32:33], 0, s[0:1]
	v_lshl_add_u64 v[36:37], v[34:35], 0, s[0:1]
	v_lshl_add_u64 v[38:39], v[36:37], 0, s[0:1]
	v_lshl_add_u64 v[40:41], v[38:39], 0, s[0:1]
	global_load_dword v4, v[26:27], off nt
	s_nop 0
	global_load_dword v28, v[28:29], off nt
	s_nop 0
	global_load_dword v29, v[30:31], off nt
	s_nop 0
	global_load_dword v30, v[32:33], off nt
	global_load_dword v31, v[34:35], off nt
	s_nop 0
	global_load_dword v32, v[36:37], off nt
	global_load_dword v33, v[38:39], off nt
	global_load_dword v34, v[40:41], off nt
	v_lshl_add_u64 v[26:27], v[40:41], 0, s[0:1]
	global_load_dword v35, v[26:27], off nt
	v_lshl_add_u64 v[26:27], v[26:27], 0, s[0:1]
	global_load_dword v36, v[26:27], off nt
	v_lshl_add_u64 v[26:27], v[26:27], 0, s[0:1]
	global_load_dword v37, v[26:27], off nt
	v_lshl_add_u64 v[26:27], v[26:27], 0, s[0:1]
	global_load_dword v38, v[26:27], off nt
	v_lshl_add_u64 v[26:27], v[26:27], 0, s[0:1]
	global_load_dword v39, v[26:27], off nt
	v_lshl_add_u64 v[26:27], v[26:27], 0, s[0:1]
	global_load_dword v40, v[26:27], off nt
	v_lshl_add_u64 v[26:27], v[26:27], 0, s[0:1]
	global_load_dword v41, v[26:27], off nt
	v_lshl_add_u64 v[26:27], v[26:27], 0, s[0:1]
	global_load_dword v42, v[26:27], off nt
	v_lshl_add_u64 v[26:27], v[26:27], 0, s[0:1]
	global_load_dword v43, v[26:27], off nt
	v_lshl_add_u64 v[26:27], v[26:27], 0, s[0:1]
	global_load_dword v44, v[26:27], off nt
	v_lshl_add_u64 v[26:27], v[26:27], 0, s[0:1]
	global_load_dword v45, v[26:27], off nt
	v_lshl_add_u64 v[26:27], v[26:27], 0, s[0:1]
	global_load_dword v46, v[26:27], off nt
	v_lshl_add_u64 v[26:27], v[26:27], 0, s[0:1]
	global_load_dword v47, v[26:27], off nt
	v_lshl_add_u64 v[26:27], v[26:27], 0, s[0:1]
	global_load_dword v48, v[26:27], off nt
	v_lshl_add_u64 v[26:27], v[26:27], 0, s[0:1]
	global_load_dword v49, v[26:27], off nt
	v_lshl_add_u64 v[26:27], v[26:27], 0, s[0:1]
	global_load_dword v50, v[26:27], off nt
	v_lshl_add_u64 v[26:27], v[26:27], 0, s[0:1]
	global_load_dword v51, v[26:27], off nt
	v_lshl_add_u64 v[26:27], v[26:27], 0, s[0:1]
	global_load_dword v52, v[26:27], off nt
	v_lshl_add_u64 v[26:27], v[26:27], 0, s[0:1]
	global_load_dword v53, v[26:27], off nt
	v_lshl_add_u64 v[26:27], v[26:27], 0, s[0:1]
	global_load_dword v54, v[26:27], off nt
	v_lshl_add_u64 v[26:27], v[26:27], 0, s[0:1]
	global_load_dword v55, v[26:27], off nt
	v_lshl_add_u64 v[26:27], v[26:27], 0, s[0:1]
	global_load_dword v56, v[26:27], off nt
	v_lshl_add_u64 v[26:27], v[26:27], 0, s[0:1]
	global_load_dword v57, v[26:27], off nt
	v_lshl_add_u64 v[26:27], v[26:27], 0, s[0:1]
	global_load_dword v26, v[26:27], off nt
	s_ashr_i32 s5, s4, 31
	s_lshl_b64 s[4:5], s[4:5], 1
	s_add_i32 s16, s16, s17
	s_add_i32 s23, s23, s24
	s_add_i32 s25, s25, s26
	s_cmpk_lt_i32 s16, 0x880
	s_waitcnt vmcnt(31)
	v_cndmask_b32_e64 v4, 0, v4, s[6:7]
	s_waitcnt vmcnt(30)
	v_cndmask_b32_e64 v27, 0, v28, s[6:7]
	ds_write2_b32 v18, v4, v27 offset1:66
	s_waitcnt vmcnt(29)
	v_cndmask_b32_e64 v4, 0, v29, s[6:7]
	s_waitcnt vmcnt(28)
	v_cndmask_b32_e64 v27, 0, v30, s[6:7]
	ds_write2_b32 v18, v4, v27 offset0:132 offset1:198
	s_waitcnt vmcnt(27)
	v_cndmask_b32_e64 v4, 0, v31, s[6:7]
	s_waitcnt vmcnt(26)
	v_cndmask_b32_e64 v27, 0, v32, s[6:7]
	ds_write2_b32 v19, v4, v27 offset0:8 offset1:74
	s_waitcnt vmcnt(25)
	v_cndmask_b32_e64 v4, 0, v33, s[6:7]
	s_waitcnt vmcnt(24)
	v_cndmask_b32_e64 v27, 0, v34, s[6:7]
	ds_write2_b32 v19, v4, v27 offset0:140 offset1:206
	s_waitcnt vmcnt(23)
	v_cndmask_b32_e64 v4, 0, v35, s[6:7]
	s_waitcnt vmcnt(22)
	v_cndmask_b32_e64 v27, 0, v36, s[6:7]
	ds_write2_b32 v20, v4, v27 offset0:16 offset1:82
	s_waitcnt vmcnt(21)
	v_cndmask_b32_e64 v4, 0, v37, s[6:7]
	s_waitcnt vmcnt(20)
	v_cndmask_b32_e64 v27, 0, v38, s[6:7]
	ds_write2_b32 v20, v4, v27 offset0:148 offset1:214
	s_waitcnt vmcnt(19)
	v_cndmask_b32_e64 v4, 0, v39, s[6:7]
	s_waitcnt vmcnt(18)
	v_cndmask_b32_e64 v27, 0, v40, s[6:7]
	ds_write2_b32 v21, v4, v27 offset0:24 offset1:90
	s_waitcnt vmcnt(17)
	v_cndmask_b32_e64 v4, 0, v41, s[6:7]
	s_waitcnt vmcnt(16)
	v_cndmask_b32_e64 v27, 0, v42, s[6:7]
	ds_write2_b32 v21, v4, v27 offset0:156 offset1:222
	s_waitcnt vmcnt(15)
	v_cndmask_b32_e64 v4, 0, v43, s[6:7]
	s_waitcnt vmcnt(14)
	v_cndmask_b32_e64 v27, 0, v44, s[6:7]
	ds_write2_b32 v22, v4, v27 offset0:32 offset1:98
	s_waitcnt vmcnt(13)
	v_cndmask_b32_e64 v4, 0, v45, s[6:7]
	s_waitcnt vmcnt(12)
	v_cndmask_b32_e64 v27, 0, v46, s[6:7]
	ds_write2_b32 v22, v4, v27 offset0:164 offset1:230
	s_waitcnt vmcnt(11)
	v_cndmask_b32_e64 v4, 0, v47, s[6:7]
	v_lshl_add_u64 v[46:47], s[2:3], 0, v[6:7]
	s_waitcnt vmcnt(10)
	v_cndmask_b32_e64 v27, 0, v48, s[6:7]
	ds_write2_b32 v23, v4, v27 offset0:40 offset1:106
	s_waitcnt vmcnt(9)
	v_cndmask_b32_e64 v4, 0, v49, s[6:7]
	v_lshl_add_u64 v[46:47], v[46:47], 0, s[4:5]
	s_waitcnt vmcnt(8)
	v_cndmask_b32_e64 v27, 0, v50, s[6:7]
	ds_write2_b32 v23, v4, v27 offset0:172 offset1:238
	s_waitcnt vmcnt(7)
	v_cndmask_b32_e64 v4, 0, v51, s[6:7]
	v_lshl_add_u64 v[46:47], v[46:47], 0, v[14:15]
	s_waitcnt vmcnt(6)
	v_cndmask_b32_e64 v27, 0, v52, s[6:7]
	ds_write2_b32 v24, v4, v27 offset0:48 offset1:114
	s_waitcnt vmcnt(5)
	v_cndmask_b32_e64 v4, 0, v53, s[6:7]
	s_waitcnt vmcnt(4)
	v_cndmask_b32_e64 v27, 0, v54, s[6:7]
	ds_write2_b32 v24, v4, v27 offset0:180 offset1:246
	s_waitcnt vmcnt(3)
	v_cndmask_b32_e64 v4, 0, v55, s[6:7]
	s_waitcnt vmcnt(2)
	v_cndmask_b32_e64 v27, 0, v56, s[6:7]
	ds_write2_b32 v25, v4, v27 offset0:56 offset1:122
	s_waitcnt vmcnt(1)
	v_cndmask_b32_e64 v4, 0, v57, s[6:7]
	s_waitcnt vmcnt(0)
	v_cndmask_b32_e64 v26, 0, v26, s[6:7]
	ds_write2_b32 v25, v4, v26 offset0:188 offset1:254
	s_waitcnt lgkmcnt(0)
	ds_read2_b32 v[30:31], v16 offset0:33 offset1:41
	ds_read2_b32 v[32:33], v16 offset1:8
	ds_read2_b32 v[34:35], v16 offset0:66 offset1:74
	ds_read2_b32 v[36:37], v16 offset0:99 offset1:107
	ds_read2_b32 v[38:39], v16 offset0:132 offset1:140
	ds_read2_b32 v[40:41], v16 offset0:165 offset1:173
	ds_read2_b32 v[42:43], v16 offset0:198 offset1:206
	ds_read2_b32 v[44:45], v16 offset0:231 offset1:239
	s_waitcnt lgkmcnt(6)
	v_cvt_pk_bf16_f32 v26, v32, v30
	s_waitcnt lgkmcnt(4)
	v_cvt_pk_bf16_f32 v27, v34, v36
	s_waitcnt lgkmcnt(2)
	v_cvt_pk_bf16_f32 v28, v38, v40
	s_waitcnt lgkmcnt(0)
	v_cvt_pk_bf16_f32 v29, v42, v44
	global_store_dwordx4 v[46:47], v[26:29], off
	s_nop 1
	v_cvt_pk_bf16_f32 v26, v33, v31
	v_cvt_pk_bf16_f32 v27, v35, v37
	v_cvt_pk_bf16_f32 v28, v39, v41
	v_cvt_pk_bf16_f32 v29, v43, v45
	v_lshl_add_u64 v[30:31], s[2:3], 0, v[8:9]
	ds_read2_b32 v[32:33], v16 offset0:49 offset1:57
	ds_read2_b32 v[34:35], v16 offset0:16 offset1:24
	ds_read2_b32 v[36:37], v16 offset0:82 offset1:90
	ds_read2_b32 v[38:39], v16 offset0:115 offset1:123
	ds_read2_b32 v[40:41], v16 offset0:148 offset1:156
	ds_read2_b32 v[42:43], v16 offset0:181 offset1:189
	ds_read2_b32 v[44:45], v16 offset0:214 offset1:222
	ds_read2_b32 v[46:47], v16 offset0:247 offset1:255
	v_lshl_add_u64 v[30:31], v[30:31], 0, s[4:5]
	v_lshl_add_u64 v[30:31], v[30:31], 0, v[14:15]
	global_store_dwordx4 v[30:31], v[26:29], off
	v_lshl_add_u64 v[30:31], s[2:3], 0, v[10:11]
	v_lshl_add_u64 v[30:31], v[30:31], 0, s[4:5]
	s_waitcnt lgkmcnt(6)
	v_cvt_pk_bf16_f32 v26, v34, v32
	s_waitcnt lgkmcnt(4)
	v_cvt_pk_bf16_f32 v27, v36, v38
	s_waitcnt lgkmcnt(2)
	v_cvt_pk_bf16_f32 v28, v40, v42
	s_waitcnt lgkmcnt(0)
	v_cvt_pk_bf16_f32 v29, v44, v46
	v_lshl_add_u64 v[30:31], v[30:31], 0, v[14:15]
	global_store_dwordx4 v[30:31], v[26:29], off
	v_lshl_add_u64 v[30:31], s[2:3], 0, v[12:13]
	v_lshl_add_u64 v[30:31], v[30:31], 0, s[4:5]
	v_cvt_pk_bf16_f32 v26, v35, v33
	v_cvt_pk_bf16_f32 v27, v37, v39
	v_cvt_pk_bf16_f32 v28, v41, v43
	v_cvt_pk_bf16_f32 v29, v45, v47
	v_lshl_add_u64 v[30:31], v[30:31], 0, v[14:15]
	global_store_dwordx4 v[30:31], v[26:29], off
	s_waitcnt lgkmcnt(0)
	s_cbranch_scc0 .LBB0_17

.LBB0_169:
	v_bfe_u32 v12, v1, 5, 1
	v_add_u32_e32 v2, s1, v12
	v_mad_i64_i32 v[2:3], s[0:1], s10, v2, 0
	v_lshl_add_u64 v[2:3], v[2:3], 2, s[4:5]
	s_ashr_i32 s3, s2, 31
	v_and_b32_e32 v24, 31, v1
	v_lshl_add_u64 v[2:3], s[2:3], 2, v[2:3]
	v_lshlrev_b32_e32 v34, 2, v24
	s_mov_b32 s2, 0
	v_lshl_add_u64 v[2:3], v[2:3], 0, v[34:35]
	s_lshl_b32 s0, s10, 3
	s_mov_b32 s3, 1
	s_mov_b32 s1, s2
	v_lshl_add_u64 v[4:5], v[2:3], 0, s[0:1]
	v_lshl_add_u64 v[6:7], v[4:5], 0, s[0:1]
	v_lshl_add_u64 v[8:9], v[6:7], 0, s[0:1]
	v_lshl_add_u64 v[10:11], v[8:9], 0, s[0:1]
	v_lshl_add_u64 v[20:21], v[10:11], 0, s[0:1]
	v_lshl_add_u64 v[22:23], v[20:21], 0, s[0:1]
	v_lshl_add_u64 v[26:27], v[22:23], 0, s[0:1]
	global_load_dword v14, v[2:3], off nt
	global_load_dword v15, v[4:5], off nt
	global_load_dword v16, v[6:7], off nt
	global_load_dword v17, v[8:9], off nt
	global_load_dword v18, v[10:11], off nt
	s_nop 0
	global_load_dword v20, v[20:21], off nt
	s_nop 0
	global_load_dword v19, v[22:23], off nt
	global_load_dword v21, v[26:27], off nt
	v_lshl_add_u64 v[2:3], v[26:27], 0, s[0:1]
	global_load_dword v22, v[2:3], off nt
	v_lshl_add_u64 v[2:3], v[2:3], 0, s[0:1]
	global_load_dword v32, v[2:3], off nt
	v_lshl_add_u64 v[2:3], v[2:3], 0, s[0:1]
	global_load_dword v33, v[2:3], off nt
	v_lshl_add_u64 v[2:3], v[2:3], 0, s[0:1]
	global_load_dword v38, v[2:3], off nt
	v_lshl_add_u64 v[2:3], v[2:3], 0, s[0:1]
	global_load_dword v40, v[2:3], off nt
	v_lshl_add_u64 v[2:3], v[2:3], 0, s[0:1]
	global_load_dword v43, v[2:3], off nt
	v_lshl_add_u64 v[2:3], v[2:3], 0, s[0:1]
	global_load_dword v44, v[2:3], off nt
	v_lshl_add_u64 v[2:3], v[2:3], 0, s[0:1]
	global_load_dword v47, v[2:3], off nt
	v_lshl_add_u64 v[2:3], v[2:3], 0, s[0:1]
	global_load_dword v49, v[2:3], off nt
	v_lshl_add_u64 v[2:3], v[2:3], 0, s[0:1]
	global_load_dword v52, v[2:3], off nt
	v_lshl_add_u64 v[2:3], v[2:3], 0, s[0:1]
	global_load_dword v53, v[2:3], off nt
	v_lshl_add_u64 v[2:3], v[2:3], 0, s[0:1]
	global_load_dword v56, v[2:3], off nt
	v_lshl_add_u64 v[2:3], v[2:3], 0, s[0:1]
	global_load_dword v58, v[2:3], off nt
	v_lshl_add_u64 v[2:3], v[2:3], 0, s[0:1]
	global_load_dword v61, v[2:3], off nt
	v_lshl_add_u64 v[2:3], v[2:3], 0, s[0:1]
	global_load_dword v62, v[2:3], off nt
	v_lshl_add_u64 v[2:3], v[2:3], 0, s[0:1]
	global_load_dword v65, v[2:3], off nt
	v_lshl_add_u64 v[2:3], v[2:3], 0, s[0:1]
	global_load_dword v67, v[2:3], off nt
	v_lshl_add_u64 v[2:3], v[2:3], 0, s[0:1]
	global_load_dword v70, v[2:3], off nt
	v_lshl_add_u64 v[2:3], v[2:3], 0, s[0:1]
	global_load_dword v71, v[2:3], off nt
	v_lshl_add_u64 v[2:3], v[2:3], 0, s[0:1]
	global_load_dword v74, v[2:3], off nt
	v_lshl_add_u64 v[2:3], v[2:3], 0, s[0:1]
	global_load_dword v76, v[2:3], off nt
	v_lshl_add_u64 v[2:3], v[2:3], 0, s[0:1]
	global_load_dword v77, v[2:3], off nt
	v_lshl_add_u64 v[2:3], v[2:3], 0, s[0:1]
	global_load_dword v78, v[2:3], off nt
	v_lshl_add_u64 v[2:3], v[2:3], 0, s[0:1]
	global_load_dword v79, v[2:3], off nt
	v_readlane_b32 s4, v255, 37
	s_lshl_b32 s0, s26, 14
	v_readlane_b32 s5, v255, 38
	v_readlane_b32 s36, v252, 48
	s_add_i32 s0, s0, 0
	s_lshl_b64 s[2:3], s[4:5], 15
	s_lshl_b64 s[4:5], s[4:5], 16
	v_readlane_b32 s40, v252, 52
	v_readlane_b32 s41, v252, 53
	s_add_u32 s26, s40, s6
	v_bfe_u32 v4, v1, 3, 3
	v_lshlrev_b32_e32 v1, 3, v1
	s_addc_u32 s28, s41, s7
	v_and_b32_e32 v2, 56, v1
	v_readlane_b32 s37, v252, 49
	v_add_u32_e32 v13, s0, v34
	v_mul_u32_u24_e32 v23, 0x84, v12
	s_add_u32 s29, s36, s8
	v_mul_u32_u24_e32 v1, 0x84, v2
	v_lshlrev_b32_e32 v5, 2, v4
	v_lshlrev_b32_e32 v4, 10, v4
	s_addc_u32 s30, s37, s9
	v_mov_b32_e32 v3, v35
	v_add3_u32 v1, s0, v1, v5
	v_mov_b32_e32 v5, v35
	v_or_b32_e32 v6, 0x2000, v4
	v_mov_b32_e32 v7, v35
	v_or_b32_e32 v8, 0x4000, v4
	v_mov_b32_e32 v9, v35
	v_or_b32_e32 v10, 0x6000, v4
	v_mov_b32_e32 v11, v35
	s_lshl_b32 s31, s27, 5
	s_lshl_b32 s34, s49, 5
	s_lshl_b32 s35, s27, 1
	s_lshl_b32 s36, s49, 1
	v_lshlrev_b32_e32 v34, 2, v24
	v_add_u32_e32 v13, v13, v23
	v_readlane_b32 s38, v252, 50
	v_readlane_b32 s39, v252, 51
	v_readlane_b32 s42, v252, 54
	v_readlane_b32 s43, v252, 55
	s_branch .LBB0_171

.LBB0_180:
	v_add_u32_e32 v23, s1, v12
	v_mad_i64_i32 v[24:25], s[0:1], s24, v23, 0
	v_lshl_add_u64 v[24:25], v[24:25], 2, s[22:23]
	s_ashr_i32 s19, s18, 31
	v_lshl_add_u64 v[24:25], s[18:19], 2, v[24:25]
	s_mov_b32 s18, 0
	v_lshl_add_u64 v[24:25], v[24:25], 0, v[34:35]
	s_lshl_b32 s0, s24, 3
	s_mov_b32 s19, 1
	s_mov_b32 s1, s18
	v_lshl_add_u64 v[26:27], v[24:25], 0, s[0:1]
	v_lshl_add_u64 v[28:29], v[26:27], 0, s[0:1]
	v_lshl_add_u64 v[30:31], v[28:29], 0, s[0:1]
	v_lshl_add_u64 v[36:37], v[30:31], 0, s[0:1]
	v_lshl_add_u64 v[50:51], v[36:37], 0, s[0:1]
	v_lshl_add_u64 v[54:55], v[50:51], 0, s[0:1]
	v_lshl_add_u64 v[68:69], v[54:55], 0, s[0:1]
	global_load_dword v23, v[24:25], off nt
	s_nop 0
	global_load_dword v24, v[26:27], off nt
	global_load_dword v25, v[28:29], off nt
	s_nop 0
	global_load_dword v26, v[30:31], off nt
	global_load_dword v27, v[36:37], off nt
	global_load_dword v28, v[50:51], off nt
	global_load_dword v29, v[54:55], off nt
	s_nop 0
	global_load_dword v30, v[68:69], off nt
	v_lshl_add_u64 v[36:37], v[68:69], 0, s[0:1]
	v_lshl_add_u64 v[50:51], v[36:37], 0, s[0:1]
	global_load_dword v31, v[36:37], off nt
	s_nop 0
	global_load_dword v36, v[50:51], off nt
	v_lshl_add_u64 v[50:51], v[50:51], 0, s[0:1]
	global_load_dword v37, v[50:51], off nt
	v_lshl_add_u64 v[50:51], v[50:51], 0, s[0:1]
	global_load_dword v39, v[50:51], off nt
	v_lshl_add_u64 v[50:51], v[50:51], 0, s[0:1]
	global_load_dword v41, v[50:51], off nt
	v_lshl_add_u64 v[50:51], v[50:51], 0, s[0:1]
	global_load_dword v42, v[50:51], off nt
	v_lshl_add_u64 v[50:51], v[50:51], 0, s[0:1]
	global_load_dword v45, v[50:51], off nt
	v_lshl_add_u64 v[50:51], v[50:51], 0, s[0:1]
	global_load_dword v46, v[50:51], off nt
	v_lshl_add_u64 v[50:51], v[50:51], 0, s[0:1]
	v_lshl_add_u64 v[54:55], v[50:51], 0, s[0:1]
	global_load_dword v48, v[50:51], off nt
	s_nop 0
	global_load_dword v50, v[54:55], off nt
	v_lshl_add_u64 v[54:55], v[54:55], 0, s[0:1]
	v_lshl_add_u64 v[68:69], v[54:55], 0, s[0:1]
	global_load_dword v51, v[54:55], off nt
	s_nop 0
	global_load_dword v54, v[68:69], off nt
	v_lshl_add_u64 v[68:69], v[68:69], 0, s[0:1]
	global_load_dword v55, v[68:69], off nt
	v_lshl_add_u64 v[68:69], v[68:69], 0, s[0:1]
	global_load_dword v57, v[68:69], off nt
	v_lshl_add_u64 v[68:69], v[68:69], 0, s[0:1]
	global_load_dword v59, v[68:69], off nt
	v_lshl_add_u64 v[68:69], v[68:69], 0, s[0:1]
	global_load_dword v60, v[68:69], off nt
	v_lshl_add_u64 v[68:69], v[68:69], 0, s[0:1]
	global_load_dword v63, v[68:69], off nt
	v_lshl_add_u64 v[68:69], v[68:69], 0, s[0:1]
	global_load_dword v64, v[68:69], off nt
	v_lshl_add_u64 v[68:69], v[68:69], 0, s[0:1]
	v_lshl_add_u64 v[72:73], v[68:69], 0, s[0:1]
	global_load_dword v66, v[68:69], off nt
	s_nop 0
	global_load_dword v68, v[72:73], off nt
	v_lshl_add_u64 v[72:73], v[72:73], 0, s[0:1]
	v_lshl_add_u64 v[80:81], v[72:73], 0, s[0:1]
	global_load_dword v69, v[72:73], off nt
	s_nop 0
	global_load_dword v72, v[80:81], off nt
	v_lshl_add_u64 v[80:81], v[80:81], 0, s[0:1]
	global_load_dword v73, v[80:81], off nt
	v_lshl_add_u64 v[80:81], v[80:81], 0, s[0:1]
	global_load_dword v75, v[80:81], off nt

.LBB0_629:
	v_lshrrev_b32_e32 v12, 5, v140
	v_add_u32_e32 v2, s1, v12
	v_mad_i64_i32 v[2:3], s[0:1], s8, v2, 0
	v_lshl_add_u64 v[2:3], v[2:3], 2, s[4:5]
	s_ashr_i32 s3, s2, 31
	v_and_b32_e32 v14, 31, v1
	v_lshl_add_u64 v[2:3], s[2:3], 2, v[2:3]
	v_lshlrev_b32_e32 v34, 2, v14
	s_mov_b32 s0, 0
	v_lshl_add_u64 v[2:3], v[2:3], 0, v[34:35]
	s_lshl_b32 s2, s8, 3
	s_mov_b32 s1, 1
	s_mov_b32 s3, s0
	global_load_dword v15, v[2:3], off nt
	v_lshl_add_u64 v[2:3], v[2:3], 0, s[2:3]
	global_load_dword v16, v[2:3], off nt
	v_lshl_add_u64 v[2:3], v[2:3], 0, s[2:3]
	global_load_dword v17, v[2:3], off nt
	v_lshl_add_u64 v[2:3], v[2:3], 0, s[2:3]
	global_load_dword v18, v[2:3], off nt
	v_lshl_add_u64 v[2:3], v[2:3], 0, s[2:3]
	global_load_dword v19, v[2:3], off nt
	v_lshl_add_u64 v[2:3], v[2:3], 0, s[2:3]
	global_load_dword v20, v[2:3], off nt
	v_lshl_add_u64 v[2:3], v[2:3], 0, s[2:3]
	global_load_dword v21, v[2:3], off nt
	v_lshl_add_u64 v[2:3], v[2:3], 0, s[2:3]
	global_load_dword v26, v[2:3], off nt
	v_lshl_add_u64 v[2:3], v[2:3], 0, s[2:3]
	global_load_dword v27, v[2:3], off nt
	v_lshl_add_u64 v[2:3], v[2:3], 0, s[2:3]
	global_load_dword v28, v[2:3], off nt
	v_lshl_add_u64 v[2:3], v[2:3], 0, s[2:3]
	global_load_dword v29, v[2:3], off nt
	v_lshl_add_u64 v[2:3], v[2:3], 0, s[2:3]
	global_load_dword v31, v[2:3], off nt
	v_lshl_add_u64 v[2:3], v[2:3], 0, s[2:3]
	global_load_dword v32, v[2:3], off nt
	v_lshl_add_u64 v[2:3], v[2:3], 0, s[2:3]
	global_load_dword v36, v[2:3], off nt
	v_lshl_add_u64 v[2:3], v[2:3], 0, s[2:3]
	global_load_dword v37, v[2:3], off nt
	v_lshl_add_u64 v[2:3], v[2:3], 0, s[2:3]
	global_load_dword v38, v[2:3], off nt
	v_lshl_add_u64 v[2:3], v[2:3], 0, s[2:3]
	global_load_dword v39, v[2:3], off nt
	v_lshl_add_u64 v[2:3], v[2:3], 0, s[2:3]
	global_load_dword v41, v[2:3], off nt
	v_lshl_add_u64 v[2:3], v[2:3], 0, s[2:3]
	global_load_dword v42, v[2:3], off nt
	v_lshl_add_u64 v[2:3], v[2:3], 0, s[2:3]
	global_load_dword v43, v[2:3], off nt
	v_lshl_add_u64 v[2:3], v[2:3], 0, s[2:3]
	global_load_dword v44, v[2:3], off nt
	v_lshl_add_u64 v[2:3], v[2:3], 0, s[2:3]
	global_load_dword v45, v[2:3], off nt
	v_lshl_add_u64 v[2:3], v[2:3], 0, s[2:3]
	global_load_dword v46, v[2:3], off nt
	v_lshl_add_u64 v[2:3], v[2:3], 0, s[2:3]
	global_load_dword v47, v[2:3], off nt
	v_lshl_add_u64 v[2:3], v[2:3], 0, s[2:3]
	global_load_dword v48, v[2:3], off nt
	v_lshl_add_u64 v[2:3], v[2:3], 0, s[2:3]
	global_load_dword v49, v[2:3], off nt
	v_lshl_add_u64 v[2:3], v[2:3], 0, s[2:3]
	global_load_dword v50, v[2:3], off nt
	v_lshl_add_u64 v[2:3], v[2:3], 0, s[2:3]
	global_load_dword v51, v[2:3], off nt
	v_lshl_add_u64 v[2:3], v[2:3], 0, s[2:3]
	global_load_dword v52, v[2:3], off nt
	v_lshl_add_u64 v[2:3], v[2:3], 0, s[2:3]
	global_load_dword v53, v[2:3], off nt
	v_lshl_add_u64 v[2:3], v[2:3], 0, s[2:3]
	global_load_dword v54, v[2:3], off nt
	v_lshl_add_u64 v[2:3], v[2:3], 0, s[2:3]
	global_load_dword v55, v[2:3], off nt
	v_readlane_b32 s6, v255, 37
	v_readlane_b32 s7, v255, 38
	v_readlane_b32 s36, v252, 48
	s_lshl_b64 s[2:3], s[6:7], 15
	s_lshl_b64 s[4:5], s[6:7], 16
	s_lshl_b64 s[0:1], s[6:7], 27
	s_lshl_b64 s[8:9], s[6:7], 28
	v_readlane_b32 s40, v252, 52
	v_readlane_b32 s41, v252, 53
	s_add_u32 s34, s40, s0
	v_lshlrev_b32_e32 v2, 3, v140
	s_addc_u32 s35, s41, s1
	v_lshrrev_b32_e32 v4, 3, v140
	v_and_b32_e32 v2, 56, v2
	v_readlane_b32 s37, v252, 49
	v_readlane_b32 s38, v252, 50
	v_readlane_b32 s39, v252, 51
	v_add_u32_e32 v22, s28, v34
	v_mul_u32_u24_e32 v23, 0x84, v12
	s_add_u32 s36, s36, s8
	v_mul_u32_u24_e32 v5, 0x84, v2
	v_lshlrev_b32_e32 v6, 2, v4
	v_lshlrev_b32_e32 v4, 10, v4
	s_addc_u32 s37, s37, s9
	v_mov_b32_e32 v3, v35
	v_add3_u32 v13, s28, v5, v6
	v_mov_b32_e32 v5, v35
	v_or_b32_e32 v6, 0x2000, v4
	v_mov_b32_e32 v7, v35
	v_or_b32_e32 v8, 0x4000, v4
	v_mov_b32_e32 v9, v35
	v_or_b32_e32 v10, 0x6000, v4
	v_mov_b32_e32 v11, v35
	s_lshl_b32 s38, s31, 5
	s_lshl_b32 s39, s52, 5
	s_lshl_b32 s40, s31, 1
	s_lshl_b32 s41, s52, 1
	v_lshlrev_b32_e32 v34, 2, v14
	v_add_u32_e32 v14, v22, v23
	v_readlane_b32 s42, v252, 54
	v_readlane_b32 s43, v252, 55
	s_branch .LBB0_631

.LBB0_640:
	v_add_u32_e32 v22, s1, v12
	v_mad_i64_i32 v[22:23], s[0:1], s26, v22, 0
	v_lshl_add_u64 v[22:23], v[22:23], 2, s[24:25]
	s_ashr_i32 s23, s22, 31
	v_lshl_add_u64 v[22:23], s[22:23], 2, v[22:23]
	s_mov_b32 s0, 0
	v_lshl_add_u64 v[24:25], v[22:23], 0, v[34:35]
	s_lshl_b32 s22, s26, 3
	s_mov_b32 s1, 1
	s_mov_b32 s23, s0
	global_load_dword v22, v[24:25], off nt
	v_lshl_add_u64 v[24:25], v[24:25], 0, s[22:23]
	v_lshl_add_u64 v[56:57], v[24:25], 0, s[22:23]
	global_load_dword v23, v[24:25], off nt
	s_nop 0
	global_load_dword v24, v[56:57], off nt
	v_lshl_add_u64 v[56:57], v[56:57], 0, s[22:23]
	global_load_dword v25, v[56:57], off nt
	v_lshl_add_u64 v[56:57], v[56:57], 0, s[22:23]
	global_load_dword v30, v[56:57], off nt
	v_lshl_add_u64 v[56:57], v[56:57], 0, s[22:23]
	global_load_dword v33, v[56:57], off nt
	v_lshl_add_u64 v[56:57], v[56:57], 0, s[22:23]
	v_lshl_add_u64 v[58:59], v[56:57], 0, s[22:23]
	global_load_dword v40, v[56:57], off nt
	s_nop 0
	global_load_dword v56, v[58:59], off nt
	v_lshl_add_u64 v[58:59], v[58:59], 0, s[22:23]
	v_lshl_add_u64 v[60:61], v[58:59], 0, s[22:23]
	global_load_dword v57, v[58:59], off nt
	s_nop 0
	global_load_dword v58, v[60:61], off nt
	v_lshl_add_u64 v[60:61], v[60:61], 0, s[22:23]
	v_lshl_add_u64 v[62:63], v[60:61], 0, s[22:23]
	global_load_dword v59, v[60:61], off nt
	s_nop 0
	global_load_dword v60, v[62:63], off nt
	v_lshl_add_u64 v[62:63], v[62:63], 0, s[22:23]
	v_lshl_add_u64 v[64:65], v[62:63], 0, s[22:23]
	global_load_dword v61, v[62:63], off nt
	s_nop 0
	global_load_dword v62, v[64:65], off nt
	v_lshl_add_u64 v[64:65], v[64:65], 0, s[22:23]
	v_lshl_add_u64 v[66:67], v[64:65], 0, s[22:23]
	global_load_dword v63, v[64:65], off nt
	s_nop 0
	global_load_dword v64, v[66:67], off nt
	v_lshl_add_u64 v[66:67], v[66:67], 0, s[22:23]
	v_lshl_add_u64 v[68:69], v[66:67], 0, s[22:23]
	global_load_dword v65, v[66:67], off nt
	s_nop 0
	global_load_dword v66, v[68:69], off nt
	v_lshl_add_u64 v[68:69], v[68:69], 0, s[22:23]
	v_lshl_add_u64 v[70:71], v[68:69], 0, s[22:23]
	global_load_dword v67, v[68:69], off nt
	s_nop 0
	global_load_dword v68, v[70:71], off nt
	v_lshl_add_u64 v[70:71], v[70:71], 0, s[22:23]
	v_lshl_add_u64 v[72:73], v[70:71], 0, s[22:23]
	global_load_dword v69, v[70:71], off nt
	s_nop 0
	global_load_dword v70, v[72:73], off nt
	v_lshl_add_u64 v[72:73], v[72:73], 0, s[22:23]
	v_lshl_add_u64 v[74:75], v[72:73], 0, s[22:23]
	global_load_dword v71, v[72:73], off nt
	s_nop 0
	global_load_dword v72, v[74:75], off nt
	v_lshl_add_u64 v[74:75], v[74:75], 0, s[22:23]
	v_lshl_add_u64 v[76:77], v[74:75], 0, s[22:23]
	global_load_dword v73, v[74:75], off nt
	s_nop 0
	global_load_dword v74, v[76:77], off nt
	v_lshl_add_u64 v[76:77], v[76:77], 0, s[22:23]
	v_lshl_add_u64 v[78:79], v[76:77], 0, s[22:23]
	global_load_dword v75, v[76:77], off nt
	s_nop 0
	global_load_dword v76, v[78:79], off nt
	v_lshl_add_u64 v[78:79], v[78:79], 0, s[22:23]
	v_lshl_add_u64 v[80:81], v[78:79], 0, s[22:23]
	global_load_dword v77, v[78:79], off nt
	s_nop 0
	global_load_dword v78, v[80:81], off nt
	v_lshl_add_u64 v[80:81], v[80:81], 0, s[22:23]
	global_load_dword v79, v[80:81], off nt
	v_lshl_add_u64 v[80:81], v[80:81], 0, s[22:23]
	global_load_dword v80, v[80:81], off nt

.LBB0_647:
	v_add_u32_e32 v13, s4, v3
	v_mad_i64_i32 v[18:19], s[18:19], s0, v13, 0
	v_lshl_add_u64 v[18:19], v[18:19], 2, s[10:11]
	v_cndmask_b32_e64 v13, 0, v2, s[8:9]
	v_lshl_add_u64 v[18:19], s[14:15], 2, v[18:19]
	v_lshlrev_b32_e32 v34, 2, v13
	s_lshl_b32 s10, s0, 3
	s_mov_b32 s0, 0
	v_lshl_add_u64 v[18:19], v[18:19], 0, v[34:35]
	s_mov_b32 s1, 1
	s_mov_b32 s11, s0
	global_load_dword v13, v[18:19], off nt
	v_lshl_add_u64 v[18:19], v[18:19], 0, s[10:11]
	global_load_dword v17, v[18:19], off nt
	v_lshl_add_u64 v[18:19], v[18:19], 0, s[10:11]
	global_load_dword v20, v[18:19], off nt
	v_lshl_add_u64 v[18:19], v[18:19], 0, s[10:11]
	global_load_dword v21, v[18:19], off nt
	v_lshl_add_u64 v[18:19], v[18:19], 0, s[10:11]
	global_load_dword v22, v[18:19], off nt
	v_lshl_add_u64 v[18:19], v[18:19], 0, s[10:11]
	global_load_dword v23, v[18:19], off nt
	v_lshl_add_u64 v[18:19], v[18:19], 0, s[10:11]
	global_load_dword v24, v[18:19], off nt
	v_lshl_add_u64 v[18:19], v[18:19], 0, s[10:11]
	global_load_dword v25, v[18:19], off nt
	v_lshl_add_u64 v[18:19], v[18:19], 0, s[10:11]
	global_load_dword v26, v[18:19], off nt
	v_lshl_add_u64 v[18:19], v[18:19], 0, s[10:11]
	global_load_dword v27, v[18:19], off nt
	v_lshl_add_u64 v[18:19], v[18:19], 0, s[10:11]
	global_load_dword v28, v[18:19], off nt
	v_lshl_add_u64 v[18:19], v[18:19], 0, s[10:11]
	global_load_dword v29, v[18:19], off nt
	v_lshl_add_u64 v[18:19], v[18:19], 0, s[10:11]
	global_load_dword v30, v[18:19], off nt
	v_lshl_add_u64 v[18:19], v[18:19], 0, s[10:11]
	global_load_dword v31, v[18:19], off nt
	v_lshl_add_u64 v[18:19], v[18:19], 0, s[10:11]
	global_load_dword v32, v[18:19], off nt
	v_lshl_add_u64 v[18:19], v[18:19], 0, s[10:11]
	global_load_dword v33, v[18:19], off nt
	v_lshl_add_u64 v[18:19], v[18:19], 0, s[10:11]
	global_load_dword v34, v[18:19], off nt
	v_lshl_add_u64 v[18:19], v[18:19], 0, s[10:11]
	global_load_dword v36, v[18:19], off nt
	v_lshl_add_u64 v[18:19], v[18:19], 0, s[10:11]
	global_load_dword v37, v[18:19], off nt
	v_lshl_add_u64 v[18:19], v[18:19], 0, s[10:11]
	global_load_dword v38, v[18:19], off nt
	v_lshl_add_u64 v[18:19], v[18:19], 0, s[10:11]
	global_load_dword v39, v[18:19], off nt
	v_lshl_add_u64 v[18:19], v[18:19], 0, s[10:11]
	global_load_dword v40, v[18:19], off nt
	v_lshl_add_u64 v[18:19], v[18:19], 0, s[10:11]
	global_load_dword v41, v[18:19], off nt
	v_lshl_add_u64 v[18:19], v[18:19], 0, s[10:11]
	global_load_dword v42, v[18:19], off nt
	v_lshl_add_u64 v[18:19], v[18:19], 0, s[10:11]
	global_load_dword v43, v[18:19], off nt
	v_lshl_add_u64 v[18:19], v[18:19], 0, s[10:11]
	global_load_dword v44, v[18:19], off nt
	v_lshl_add_u64 v[18:19], v[18:19], 0, s[10:11]
	global_load_dword v45, v[18:19], off nt
	v_lshl_add_u64 v[18:19], v[18:19], 0, s[10:11]
	global_load_dword v46, v[18:19], off nt
	v_lshl_add_u64 v[18:19], v[18:19], 0, s[10:11]
	global_load_dword v47, v[18:19], off nt
	v_lshl_add_u64 v[18:19], v[18:19], 0, s[10:11]
	global_load_dword v48, v[18:19], off nt
	v_lshl_add_u64 v[18:19], v[18:19], 0, s[10:11]
	global_load_dword v49, v[18:19], off nt
	v_lshl_add_u64 v[18:19], v[18:19], 0, s[10:11]
	global_load_dword v18, v[18:19], off nt
	v_add_u32_e32 v19, 0x400, v16
	s_ashr_i32 s5, s4, 31
	s_lshl_b64 s[0:1], s[4:5], 1
	s_add_i32 s22, s22, s52
	s_add_i32 s28, s28, s29
	s_add_i32 s30, s30, s31
	s_cmp_lt_i32 s22, s23
	s_waitcnt vmcnt(31)
	v_cndmask_b32_e64 v13, 0, v13, s[8:9]
	s_waitcnt vmcnt(30)
	v_cndmask_b32_e64 v17, 0, v17, s[8:9]
	ds_write2_b32 v16, v13, v17 offset1:66
	s_waitcnt vmcnt(29)
	v_cndmask_b32_e64 v13, 0, v20, s[8:9]
	s_waitcnt vmcnt(28)
	v_cndmask_b32_e64 v17, 0, v21, s[8:9]
	ds_write2_b32 v16, v13, v17 offset0:132 offset1:198
	s_waitcnt vmcnt(27)
	v_cndmask_b32_e64 v13, 0, v22, s[8:9]
	s_waitcnt vmcnt(26)
	v_cndmask_b32_e64 v17, 0, v23, s[8:9]
	ds_write2_b32 v19, v13, v17 offset0:8 offset1:74
	s_waitcnt vmcnt(25)
	v_cndmask_b32_e64 v13, 0, v24, s[8:9]
	s_waitcnt vmcnt(24)
	v_cndmask_b32_e64 v17, 0, v25, s[8:9]
	ds_write2_b32 v19, v13, v17 offset0:140 offset1:206
	s_waitcnt vmcnt(23)
	v_cndmask_b32_e64 v13, 0, v26, s[8:9]
	v_add_u32_e32 v19, 0x800, v16
	s_waitcnt vmcnt(22)
	v_cndmask_b32_e64 v17, 0, v27, s[8:9]
	ds_write2_b32 v19, v13, v17 offset0:16 offset1:82
	s_waitcnt vmcnt(21)
	v_cndmask_b32_e64 v13, 0, v28, s[8:9]
	s_waitcnt vmcnt(20)
	v_cndmask_b32_e64 v17, 0, v29, s[8:9]
	ds_write2_b32 v19, v13, v17 offset0:148 offset1:214
	s_waitcnt vmcnt(19)
	v_cndmask_b32_e64 v13, 0, v30, s[8:9]
	v_add_u32_e32 v19, 0xc00, v16
	s_waitcnt vmcnt(18)
	v_cndmask_b32_e64 v17, 0, v31, s[8:9]
	ds_write2_b32 v19, v13, v17 offset0:24 offset1:90
	s_waitcnt vmcnt(17)
	v_cndmask_b32_e64 v13, 0, v32, s[8:9]
	s_waitcnt vmcnt(16)
	v_cndmask_b32_e64 v17, 0, v33, s[8:9]
	ds_write2_b32 v19, v13, v17 offset0:156 offset1:222
	s_waitcnt vmcnt(15)
	v_cndmask_b32_e64 v13, 0, v34, s[8:9]
	v_add_u32_e32 v19, 0x1000, v16
	s_waitcnt vmcnt(14)
	v_cndmask_b32_e64 v17, 0, v36, s[8:9]
	ds_write2_b32 v19, v13, v17 offset0:32 offset1:98
	s_waitcnt vmcnt(13)
	v_cndmask_b32_e64 v13, 0, v37, s[8:9]
	s_waitcnt vmcnt(12)
	v_cndmask_b32_e64 v17, 0, v38, s[8:9]
	ds_write2_b32 v19, v13, v17 offset0:164 offset1:230
	s_waitcnt vmcnt(11)
	v_cndmask_b32_e64 v13, 0, v39, s[8:9]
	v_add_u32_e32 v19, 0x1400, v16
	s_waitcnt vmcnt(10)
	v_cndmask_b32_e64 v17, 0, v40, s[8:9]
	ds_write2_b32 v19, v13, v17 offset0:40 offset1:106
	s_waitcnt vmcnt(9)
	v_cndmask_b32_e64 v13, 0, v41, s[8:9]
	v_lshl_add_u64 v[40:41], s[2:3], 0, v[4:5]
	s_waitcnt vmcnt(8)
	v_cndmask_b32_e64 v17, 0, v42, s[8:9]
	ds_write2_b32 v19, v13, v17 offset0:172 offset1:238
	s_waitcnt vmcnt(7)
	v_cndmask_b32_e64 v13, 0, v43, s[8:9]
	v_add_u32_e32 v19, 0x1800, v16
	s_waitcnt vmcnt(6)
	v_cndmask_b32_e64 v17, 0, v44, s[8:9]
	ds_write2_b32 v19, v13, v17 offset0:48 offset1:114
	s_waitcnt vmcnt(5)
	v_cndmask_b32_e64 v13, 0, v45, s[8:9]
	v_lshl_add_u64 v[40:41], v[40:41], 0, s[0:1]
	s_waitcnt vmcnt(4)
	v_cndmask_b32_e64 v17, 0, v46, s[8:9]
	ds_write2_b32 v19, v13, v17 offset0:180 offset1:246
	s_waitcnt vmcnt(3)
	v_cndmask_b32_e64 v13, 0, v47, s[8:9]
	v_add_u32_e32 v19, 0x1c00, v16
	s_waitcnt vmcnt(2)
	v_cndmask_b32_e64 v17, 0, v48, s[8:9]
	ds_write2_b32 v19, v13, v17 offset0:56 offset1:122
	s_waitcnt vmcnt(1)
	v_cndmask_b32_e64 v13, 0, v49, s[8:9]
	s_waitcnt vmcnt(0)
	v_cndmask_b32_e64 v17, 0, v18, s[8:9]
	ds_write2_b32 v19, v13, v17 offset0:188 offset1:254
	s_waitcnt lgkmcnt(0)
	ds_read2_b32 v[22:23], v14 offset0:33 offset1:41
	ds_read2_b32 v[24:25], v14 offset1:8
	ds_read2_b32 v[26:27], v14 offset0:66 offset1:74
	ds_read2_b32 v[28:29], v14 offset0:99 offset1:107
	ds_read2_b32 v[30:31], v14 offset0:132 offset1:140
	ds_read2_b32 v[32:33], v14 offset0:165 offset1:173
	ds_read2_b32 v[36:37], v14 offset0:198 offset1:206
	ds_read2_b32 v[38:39], v14 offset0:231 offset1:239
	v_mov_b32_e32 v13, v35
	s_waitcnt lgkmcnt(6)
	v_cvt_pk_bf16_f32 v18, v24, v22
	s_waitcnt lgkmcnt(4)
	v_cvt_pk_bf16_f32 v19, v26, v28
	s_waitcnt lgkmcnt(2)
	v_cvt_pk_bf16_f32 v20, v30, v32
	s_waitcnt lgkmcnt(0)
	v_cvt_pk_bf16_f32 v21, v36, v38
	v_lshl_add_u64 v[40:41], v[40:41], 0, v[12:13]
	global_store_dwordx4 v[40:41], v[18:21], off
	v_lshl_add_u64 v[40:41], s[2:3], 0, v[8:9]
	v_lshl_add_u64 v[40:41], v[40:41], 0, s[0:1]
	v_cvt_pk_bf16_f32 v18, v25, v23
	v_lshl_add_u64 v[22:23], s[2:3], 0, v[6:7]
	v_lshl_add_u64 v[22:23], v[22:23], 0, s[0:1]
	v_cvt_pk_bf16_f32 v19, v27, v29
	v_cvt_pk_bf16_f32 v20, v31, v33
	v_cvt_pk_bf16_f32 v21, v37, v39
	v_lshl_add_u64 v[22:23], v[22:23], 0, v[12:13]
	global_store_dwordx4 v[22:23], v[18:21], off
	ds_read2_b32 v[22:23], v14 offset0:49 offset1:57
	ds_read2_b32 v[24:25], v14 offset0:16 offset1:24
	ds_read2_b32 v[26:27], v14 offset0:82 offset1:90
	ds_read2_b32 v[28:29], v14 offset0:115 offset1:123
	ds_read2_b32 v[30:31], v14 offset0:148 offset1:156
	ds_read2_b32 v[32:33], v14 offset0:181 offset1:189
	ds_read2_b32 v[36:37], v14 offset0:214 offset1:222
	ds_read2_b32 v[38:39], v14 offset0:247 offset1:255
	v_lshl_add_u64 v[40:41], v[40:41], 0, v[12:13]
	s_waitcnt lgkmcnt(6)
	v_cvt_pk_bf16_f32 v18, v24, v22
	s_waitcnt lgkmcnt(4)
	v_cvt_pk_bf16_f32 v19, v26, v28
	s_waitcnt lgkmcnt(2)
	v_cvt_pk_bf16_f32 v20, v30, v32
	s_waitcnt lgkmcnt(0)
	v_cvt_pk_bf16_f32 v21, v36, v38
	global_store_dwordx4 v[40:41], v[18:21], off
	s_nop 1
	v_cvt_pk_bf16_f32 v18, v25, v23
	v_lshl_add_u64 v[22:23], s[2:3], 0, v[10:11]
	v_lshl_add_u64 v[22:23], v[22:23], 0, s[0:1]
	v_cvt_pk_bf16_f32 v19, v27, v29
	v_cvt_pk_bf16_f32 v20, v31, v33
	v_cvt_pk_bf16_f32 v21, v37, v39
	v_lshl_add_u64 v[22:23], v[22:23], 0, v[12:13]
	global_store_dwordx4 v[22:23], v[18:21], off
	s_waitcnt lgkmcnt(0)
	s_cbranch_scc0 .LBB0_652

.LBB0_775:
	v_lshrrev_b32_e32 v12, 5, v140
	v_add_u32_e32 v2, s1, v12
	v_mad_i64_i32 v[2:3], s[0:1], s10, v2, 0
	v_lshl_add_u64 v[2:3], v[2:3], 2, s[8:9]
	s_ashr_i32 s5, s4, 31
	v_and_b32_e32 v14, 31, v1
	v_lshl_add_u64 v[2:3], s[4:5], 2, v[2:3]
	v_lshlrev_b32_e32 v34, 2, v14
	s_mov_b32 s0, 0
	v_lshl_add_u64 v[2:3], v[2:3], 0, v[34:35]
	s_lshl_b32 s4, s10, 3
	s_mov_b32 s1, 1
	s_mov_b32 s5, s0
	global_load_dword v15, v[2:3], off nt
	v_lshl_add_u64 v[2:3], v[2:3], 0, s[4:5]
	global_load_dword v16, v[2:3], off nt
	v_lshl_add_u64 v[2:3], v[2:3], 0, s[4:5]
	global_load_dword v17, v[2:3], off nt
	v_lshl_add_u64 v[2:3], v[2:3], 0, s[4:5]
	global_load_dword v18, v[2:3], off nt
	v_lshl_add_u64 v[2:3], v[2:3], 0, s[4:5]
	global_load_dword v19, v[2:3], off nt
	v_lshl_add_u64 v[2:3], v[2:3], 0, s[4:5]
	global_load_dword v20, v[2:3], off nt
	v_lshl_add_u64 v[2:3], v[2:3], 0, s[4:5]
	global_load_dword v21, v[2:3], off nt
	v_lshl_add_u64 v[2:3], v[2:3], 0, s[4:5]
	global_load_dword v25, v[2:3], off nt
	v_lshl_add_u64 v[2:3], v[2:3], 0, s[4:5]
	global_load_dword v26, v[2:3], off nt
	v_lshl_add_u64 v[2:3], v[2:3], 0, s[4:5]
	global_load_dword v28, v[2:3], off nt
	v_lshl_add_u64 v[2:3], v[2:3], 0, s[4:5]
	global_load_dword v29, v[2:3], off nt
	v_lshl_add_u64 v[2:3], v[2:3], 0, s[4:5]
	global_load_dword v30, v[2:3], off nt
	v_lshl_add_u64 v[2:3], v[2:3], 0, s[4:5]
	global_load_dword v32, v[2:3], off nt
	v_lshl_add_u64 v[2:3], v[2:3], 0, s[4:5]
	global_load_dword v33, v[2:3], off nt
	v_lshl_add_u64 v[2:3], v[2:3], 0, s[4:5]
	global_load_dword v36, v[2:3], off nt
	v_lshl_add_u64 v[2:3], v[2:3], 0, s[4:5]
	global_load_dword v38, v[2:3], off nt
	v_lshl_add_u64 v[2:3], v[2:3], 0, s[4:5]
	global_load_dword v39, v[2:3], off nt
	v_lshl_add_u64 v[2:3], v[2:3], 0, s[4:5]
	global_load_dword v40, v[2:3], off nt
	v_lshl_add_u64 v[2:3], v[2:3], 0, s[4:5]
	global_load_dword v41, v[2:3], off nt
	v_lshl_add_u64 v[2:3], v[2:3], 0, s[4:5]
	global_load_dword v43, v[2:3], off nt
	v_lshl_add_u64 v[2:3], v[2:3], 0, s[4:5]
	global_load_dword v44, v[2:3], off nt
	v_lshl_add_u64 v[2:3], v[2:3], 0, s[4:5]
	global_load_dword v45, v[2:3], off nt
	v_lshl_add_u64 v[2:3], v[2:3], 0, s[4:5]
	global_load_dword v46, v[2:3], off nt
	v_lshl_add_u64 v[2:3], v[2:3], 0, s[4:5]
	global_load_dword v47, v[2:3], off nt
	v_lshl_add_u64 v[2:3], v[2:3], 0, s[4:5]
	global_load_dword v48, v[2:3], off nt
	v_lshl_add_u64 v[2:3], v[2:3], 0, s[4:5]
	global_load_dword v49, v[2:3], off nt
	v_lshl_add_u64 v[2:3], v[2:3], 0, s[4:5]
	global_load_dword v50, v[2:3], off nt
	v_lshl_add_u64 v[2:3], v[2:3], 0, s[4:5]
	global_load_dword v51, v[2:3], off nt
	v_lshl_add_u64 v[2:3], v[2:3], 0, s[4:5]
	global_load_dword v52, v[2:3], off nt
	v_lshl_add_u64 v[2:3], v[2:3], 0, s[4:5]
	global_load_dword v53, v[2:3], off nt
	v_lshl_add_u64 v[2:3], v[2:3], 0, s[4:5]
	global_load_dword v54, v[2:3], off nt
	v_lshl_add_u64 v[2:3], v[2:3], 0, s[4:5]
	global_load_dword v55, v[2:3], off nt
	v_readlane_b32 s6, v255, 37
	v_readlane_b32 s7, v255, 38
	v_readlane_b32 s40, v252, 48
	s_lshl_b64 s[4:5], s[6:7], 15
	s_lshl_b64 s[8:9], s[6:7], 16
	s_lshl_b64 s[0:1], s[6:7], 27
	s_lshl_b64 s[10:11], s[6:7], 28
	v_readlane_b32 s44, v252, 52
	v_readlane_b32 s45, v252, 53
	s_add_u32 s36, s44, s0
	v_lshlrev_b32_e32 v2, 3, v140
	s_addc_u32 s37, s45, s1
	v_lshrrev_b32_e32 v4, 3, v140
	v_and_b32_e32 v2, 56, v2
	v_readlane_b32 s41, v252, 49
	v_readlane_b32 s42, v252, 50
	v_readlane_b32 s43, v252, 51
	v_add_u32_e32 v22, s30, v34
	v_mul_u32_u24_e32 v23, 0x84, v12
	s_add_u32 s38, s40, s10
	v_mul_u32_u24_e32 v5, 0x84, v2
	v_lshlrev_b32_e32 v6, 2, v4
	v_lshlrev_b32_e32 v4, 10, v4
	v_readlane_b32 s0, v253, 62
	s_addc_u32 s39, s41, s11
	v_mov_b32_e32 v3, v35
	v_add3_u32 v13, s30, v5, v6
	v_mov_b32_e32 v5, v35
	v_or_b32_e32 v6, 0x2000, v4
	v_mov_b32_e32 v7, v35
	v_or_b32_e32 v8, 0x4000, v4
	v_mov_b32_e32 v9, v35
	v_or_b32_e32 v10, 0x6000, v4
	v_mov_b32_e32 v11, v35
	s_lshl_b32 s40, s35, 5
	s_lshl_b32 s41, s0, 5
	s_lshl_b32 s42, s35, 1
	s_lshl_b32 s43, s0, 1
	v_lshlrev_b32_e32 v34, 2, v14
	v_add_u32_e32 v14, v22, v23
	v_readlane_b32 s46, v252, 54
	v_readlane_b32 s47, v252, 55
	s_branch .LBB0_777

.LBB0_786:
	v_add_u32_e32 v22, s1, v12
	v_mad_i64_i32 v[22:23], s[0:1], s28, v22, 0
	v_lshl_add_u64 v[22:23], v[22:23], 2, s[26:27]
	s_ashr_i32 s25, s24, 31
	v_lshl_add_u64 v[22:23], s[24:25], 2, v[22:23]
	s_mov_b32 s0, 0
	v_lshl_add_u64 v[56:57], v[22:23], 0, v[34:35]
	s_lshl_b32 s24, s28, 3
	s_mov_b32 s1, 1
	s_mov_b32 s25, s0
	global_load_dword v22, v[56:57], off nt
	v_lshl_add_u64 v[56:57], v[56:57], 0, s[24:25]
	global_load_dword v23, v[56:57], off nt
	v_lshl_add_u64 v[56:57], v[56:57], 0, s[24:25]
	global_load_dword v24, v[56:57], off nt
	v_lshl_add_u64 v[56:57], v[56:57], 0, s[24:25]
	global_load_dword v27, v[56:57], off nt
	v_lshl_add_u64 v[56:57], v[56:57], 0, s[24:25]
	global_load_dword v31, v[56:57], off nt
	v_lshl_add_u64 v[56:57], v[56:57], 0, s[24:25]
	global_load_dword v37, v[56:57], off nt
	v_lshl_add_u64 v[56:57], v[56:57], 0, s[24:25]
	v_lshl_add_u64 v[58:59], v[56:57], 0, s[24:25]
	global_load_dword v42, v[56:57], off nt
	s_nop 0
	global_load_dword v56, v[58:59], off nt
	v_lshl_add_u64 v[58:59], v[58:59], 0, s[24:25]
	v_lshl_add_u64 v[60:61], v[58:59], 0, s[24:25]
	global_load_dword v57, v[58:59], off nt
	s_nop 0
	global_load_dword v58, v[60:61], off nt
	v_lshl_add_u64 v[60:61], v[60:61], 0, s[24:25]
	v_lshl_add_u64 v[62:63], v[60:61], 0, s[24:25]
	global_load_dword v59, v[60:61], off nt
	s_nop 0
	global_load_dword v60, v[62:63], off nt
	v_lshl_add_u64 v[62:63], v[62:63], 0, s[24:25]
	v_lshl_add_u64 v[64:65], v[62:63], 0, s[24:25]
	global_load_dword v61, v[62:63], off nt
	s_nop 0
	global_load_dword v62, v[64:65], off nt
	v_lshl_add_u64 v[64:65], v[64:65], 0, s[24:25]
	v_lshl_add_u64 v[66:67], v[64:65], 0, s[24:25]
	global_load_dword v63, v[64:65], off nt
	s_nop 0
	global_load_dword v64, v[66:67], off nt
	v_lshl_add_u64 v[66:67], v[66:67], 0, s[24:25]
	v_lshl_add_u64 v[68:69], v[66:67], 0, s[24:25]
	global_load_dword v65, v[66:67], off nt
	s_nop 0
	global_load_dword v66, v[68:69], off nt
	v_lshl_add_u64 v[68:69], v[68:69], 0, s[24:25]
	v_lshl_add_u64 v[70:71], v[68:69], 0, s[24:25]
	global_load_dword v67, v[68:69], off nt
	s_nop 0
	global_load_dword v68, v[70:71], off nt
	v_lshl_add_u64 v[70:71], v[70:71], 0, s[24:25]
	v_lshl_add_u64 v[72:73], v[70:71], 0, s[24:25]
	global_load_dword v69, v[70:71], off nt
	s_nop 0
	global_load_dword v70, v[72:73], off nt
	v_lshl_add_u64 v[72:73], v[72:73], 0, s[24:25]
	v_lshl_add_u64 v[74:75], v[72:73], 0, s[24:25]
	global_load_dword v71, v[72:73], off nt
	s_nop 0
	global_load_dword v72, v[74:75], off nt
	v_lshl_add_u64 v[74:75], v[74:75], 0, s[24:25]
	v_lshl_add_u64 v[76:77], v[74:75], 0, s[24:25]
	global_load_dword v73, v[74:75], off nt
	s_nop 0
	global_load_dword v74, v[76:77], off nt
	v_lshl_add_u64 v[76:77], v[76:77], 0, s[24:25]
	v_lshl_add_u64 v[78:79], v[76:77], 0, s[24:25]
	global_load_dword v75, v[76:77], off nt
	s_nop 0
	global_load_dword v76, v[78:79], off nt
	v_lshl_add_u64 v[78:79], v[78:79], 0, s[24:25]
	v_lshl_add_u64 v[80:81], v[78:79], 0, s[24:25]
	global_load_dword v77, v[78:79], off nt
	s_nop 0
	global_load_dword v78, v[80:81], off nt
	v_lshl_add_u64 v[80:81], v[80:81], 0, s[24:25]
	global_load_dword v79, v[80:81], off nt
	v_lshl_add_u64 v[80:81], v[80:81], 0, s[24:25]
	global_load_dword v80, v[80:81], off nt

.LBB0_792:
	v_add_u32_e32 v13, s8, v3
	v_mad_i64_i32 v[18:19], s[22:23], s0, v13, 0
	v_lshl_add_u64 v[18:19], v[18:19], 2, s[14:15]
	v_cndmask_b32_e64 v13, 0, v2, s[10:11]
	v_lshl_add_u64 v[18:19], s[18:19], 2, v[18:19]
	v_lshlrev_b32_e32 v34, 2, v13
	s_lshl_b32 s14, s0, 3
	s_mov_b32 s0, 0
	v_lshl_add_u64 v[18:19], v[18:19], 0, v[34:35]
	s_mov_b32 s1, 1
	s_mov_b32 s15, s0
	global_load_dword v13, v[18:19], off nt
	v_lshl_add_u64 v[18:19], v[18:19], 0, s[14:15]
	global_load_dword v17, v[18:19], off nt
	v_lshl_add_u64 v[18:19], v[18:19], 0, s[14:15]
	global_load_dword v20, v[18:19], off nt
	v_lshl_add_u64 v[18:19], v[18:19], 0, s[14:15]
	global_load_dword v21, v[18:19], off nt
	v_lshl_add_u64 v[18:19], v[18:19], 0, s[14:15]
	global_load_dword v22, v[18:19], off nt
	v_lshl_add_u64 v[18:19], v[18:19], 0, s[14:15]
	global_load_dword v23, v[18:19], off nt
	v_lshl_add_u64 v[18:19], v[18:19], 0, s[14:15]
	global_load_dword v24, v[18:19], off nt
	v_lshl_add_u64 v[18:19], v[18:19], 0, s[14:15]
	global_load_dword v25, v[18:19], off nt
	v_lshl_add_u64 v[18:19], v[18:19], 0, s[14:15]
	global_load_dword v26, v[18:19], off nt
	v_lshl_add_u64 v[18:19], v[18:19], 0, s[14:15]
	global_load_dword v27, v[18:19], off nt
	v_lshl_add_u64 v[18:19], v[18:19], 0, s[14:15]
	global_load_dword v28, v[18:19], off nt
	v_lshl_add_u64 v[18:19], v[18:19], 0, s[14:15]
	global_load_dword v29, v[18:19], off nt
	v_lshl_add_u64 v[18:19], v[18:19], 0, s[14:15]
	global_load_dword v30, v[18:19], off nt
	v_lshl_add_u64 v[18:19], v[18:19], 0, s[14:15]
	global_load_dword v31, v[18:19], off nt
	v_lshl_add_u64 v[18:19], v[18:19], 0, s[14:15]
	global_load_dword v32, v[18:19], off nt
	v_lshl_add_u64 v[18:19], v[18:19], 0, s[14:15]
	global_load_dword v33, v[18:19], off nt
	v_lshl_add_u64 v[18:19], v[18:19], 0, s[14:15]
	global_load_dword v34, v[18:19], off nt
	v_lshl_add_u64 v[18:19], v[18:19], 0, s[14:15]
	global_load_dword v36, v[18:19], off nt
	v_lshl_add_u64 v[18:19], v[18:19], 0, s[14:15]
	global_load_dword v37, v[18:19], off nt
	v_lshl_add_u64 v[18:19], v[18:19], 0, s[14:15]
	global_load_dword v38, v[18:19], off nt
	v_lshl_add_u64 v[18:19], v[18:19], 0, s[14:15]
	global_load_dword v39, v[18:19], off nt
	v_lshl_add_u64 v[18:19], v[18:19], 0, s[14:15]
	global_load_dword v40, v[18:19], off nt
	v_lshl_add_u64 v[18:19], v[18:19], 0, s[14:15]
	global_load_dword v41, v[18:19], off nt
	v_lshl_add_u64 v[18:19], v[18:19], 0, s[14:15]
	global_load_dword v42, v[18:19], off nt
	v_lshl_add_u64 v[18:19], v[18:19], 0, s[14:15]
	global_load_dword v43, v[18:19], off nt
	v_lshl_add_u64 v[18:19], v[18:19], 0, s[14:15]
	global_load_dword v44, v[18:19], off nt
	v_lshl_add_u64 v[18:19], v[18:19], 0, s[14:15]
	global_load_dword v45, v[18:19], off nt
	v_lshl_add_u64 v[18:19], v[18:19], 0, s[14:15]
	global_load_dword v46, v[18:19], off nt
	v_lshl_add_u64 v[18:19], v[18:19], 0, s[14:15]
	global_load_dword v47, v[18:19], off nt
	v_lshl_add_u64 v[18:19], v[18:19], 0, s[14:15]
	global_load_dword v48, v[18:19], off nt
	v_lshl_add_u64 v[18:19], v[18:19], 0, s[14:15]
	global_load_dword v49, v[18:19], off nt
	v_lshl_add_u64 v[18:19], v[18:19], 0, s[14:15]
	global_load_dword v18, v[18:19], off nt
	v_add_u32_e32 v19, 0x400, v16
	s_ashr_i32 s9, s8, 31
	s_lshl_b64 s[0:1], s[8:9], 1
	s_add_i32 s30, s30, s31
	s_add_i32 s34, s34, s35
	s_waitcnt vmcnt(31)
	v_cndmask_b32_e64 v13, 0, v13, s[10:11]
	s_waitcnt vmcnt(30)
	v_cndmask_b32_e64 v17, 0, v17, s[10:11]
	ds_write2_b32 v16, v13, v17 offset1:66
	s_waitcnt vmcnt(29)
	v_cndmask_b32_e64 v13, 0, v20, s[10:11]
	s_waitcnt vmcnt(28)
	v_cndmask_b32_e64 v17, 0, v21, s[10:11]
	ds_write2_b32 v16, v13, v17 offset0:132 offset1:198
	s_waitcnt vmcnt(27)
	v_cndmask_b32_e64 v13, 0, v22, s[10:11]
	s_waitcnt vmcnt(26)
	v_cndmask_b32_e64 v17, 0, v23, s[10:11]
	ds_write2_b32 v19, v13, v17 offset0:8 offset1:74
	s_waitcnt vmcnt(25)
	v_cndmask_b32_e64 v13, 0, v24, s[10:11]
	s_waitcnt vmcnt(24)
	v_cndmask_b32_e64 v17, 0, v25, s[10:11]
	ds_write2_b32 v19, v13, v17 offset0:140 offset1:206
	s_waitcnt vmcnt(23)
	v_cndmask_b32_e64 v13, 0, v26, s[10:11]
	v_add_u32_e32 v19, 0x800, v16
	s_waitcnt vmcnt(22)
	v_cndmask_b32_e64 v17, 0, v27, s[10:11]
	ds_write2_b32 v19, v13, v17 offset0:16 offset1:82
	s_waitcnt vmcnt(21)
	v_cndmask_b32_e64 v13, 0, v28, s[10:11]
	s_waitcnt vmcnt(20)
	v_cndmask_b32_e64 v17, 0, v29, s[10:11]
	ds_write2_b32 v19, v13, v17 offset0:148 offset1:214
	s_waitcnt vmcnt(19)
	v_cndmask_b32_e64 v13, 0, v30, s[10:11]
	v_add_u32_e32 v19, 0xc00, v16
	s_waitcnt vmcnt(18)
	v_cndmask_b32_e64 v17, 0, v31, s[10:11]
	ds_write2_b32 v19, v13, v17 offset0:24 offset1:90
	s_waitcnt vmcnt(17)
	v_cndmask_b32_e64 v13, 0, v32, s[10:11]
	s_waitcnt vmcnt(16)
	v_cndmask_b32_e64 v17, 0, v33, s[10:11]
	ds_write2_b32 v19, v13, v17 offset0:156 offset1:222
	s_waitcnt vmcnt(15)
	v_cndmask_b32_e64 v13, 0, v34, s[10:11]
	v_add_u32_e32 v19, 0x1000, v16
	s_waitcnt vmcnt(14)
	v_cndmask_b32_e64 v17, 0, v36, s[10:11]
	ds_write2_b32 v19, v13, v17 offset0:32 offset1:98
	s_waitcnt vmcnt(13)
	v_cndmask_b32_e64 v13, 0, v37, s[10:11]
	s_waitcnt vmcnt(12)
	v_cndmask_b32_e64 v17, 0, v38, s[10:11]
	ds_write2_b32 v19, v13, v17 offset0:164 offset1:230
	s_waitcnt vmcnt(11)
	v_cndmask_b32_e64 v13, 0, v39, s[10:11]
	v_add_u32_e32 v19, 0x1400, v16
	s_waitcnt vmcnt(10)
	v_cndmask_b32_e64 v17, 0, v40, s[10:11]
	ds_write2_b32 v19, v13, v17 offset0:40 offset1:106
	s_waitcnt vmcnt(9)
	v_cndmask_b32_e64 v13, 0, v41, s[10:11]
	v_lshl_add_u64 v[40:41], s[4:5], 0, v[4:5]
	s_waitcnt vmcnt(8)
	v_cndmask_b32_e64 v17, 0, v42, s[10:11]
	ds_write2_b32 v19, v13, v17 offset0:172 offset1:238
	s_waitcnt vmcnt(7)
	v_cndmask_b32_e64 v13, 0, v43, s[10:11]
	v_add_u32_e32 v19, 0x1800, v16
	s_waitcnt vmcnt(6)
	v_cndmask_b32_e64 v17, 0, v44, s[10:11]
	ds_write2_b32 v19, v13, v17 offset0:48 offset1:114
	s_waitcnt vmcnt(5)
	v_cndmask_b32_e64 v13, 0, v45, s[10:11]
	v_lshl_add_u64 v[40:41], v[40:41], 0, s[0:1]
	s_waitcnt vmcnt(4)
	v_cndmask_b32_e64 v17, 0, v46, s[10:11]
	ds_write2_b32 v19, v13, v17 offset0:180 offset1:246
	s_waitcnt vmcnt(3)
	v_cndmask_b32_e64 v13, 0, v47, s[10:11]
	v_add_u32_e32 v19, 0x1c00, v16
	s_waitcnt vmcnt(2)
	v_cndmask_b32_e64 v17, 0, v48, s[10:11]
	ds_write2_b32 v19, v13, v17 offset0:56 offset1:122
	s_waitcnt vmcnt(1)
	v_cndmask_b32_e64 v13, 0, v49, s[10:11]
	s_waitcnt vmcnt(0)
	v_cndmask_b32_e64 v17, 0, v18, s[10:11]
	ds_write2_b32 v19, v13, v17 offset0:188 offset1:254
	s_waitcnt lgkmcnt(0)
	ds_read2_b32 v[22:23], v14 offset0:33 offset1:41
	ds_read2_b32 v[24:25], v14 offset1:8
	ds_read2_b32 v[26:27], v14 offset0:66 offset1:74
	ds_read2_b32 v[28:29], v14 offset0:99 offset1:107
	ds_read2_b32 v[30:31], v14 offset0:132 offset1:140
	ds_read2_b32 v[32:33], v14 offset0:165 offset1:173
	ds_read2_b32 v[36:37], v14 offset0:198 offset1:206
	ds_read2_b32 v[38:39], v14 offset0:231 offset1:239
	v_mov_b32_e32 v13, v35
	s_waitcnt lgkmcnt(6)
	v_cvt_pk_bf16_f32 v18, v24, v22
	s_waitcnt lgkmcnt(4)
	v_cvt_pk_bf16_f32 v19, v26, v28
	s_waitcnt lgkmcnt(2)
	v_cvt_pk_bf16_f32 v20, v30, v32
	s_waitcnt lgkmcnt(0)
	v_cvt_pk_bf16_f32 v21, v36, v38
	v_lshl_add_u64 v[40:41], v[40:41], 0, v[12:13]
	global_store_dwordx4 v[40:41], v[18:21], off
	v_lshl_add_u64 v[40:41], s[4:5], 0, v[8:9]
	v_lshl_add_u64 v[40:41], v[40:41], 0, s[0:1]
	v_cvt_pk_bf16_f32 v18, v25, v23
	v_lshl_add_u64 v[22:23], s[4:5], 0, v[6:7]
	v_lshl_add_u64 v[22:23], v[22:23], 0, s[0:1]
	v_cvt_pk_bf16_f32 v19, v27, v29
	v_cvt_pk_bf16_f32 v20, v31, v33
	v_cvt_pk_bf16_f32 v21, v37, v39
	v_lshl_add_u64 v[22:23], v[22:23], 0, v[12:13]
	global_store_dwordx4 v[22:23], v[18:21], off
	ds_read2_b32 v[22:23], v14 offset0:49 offset1:57
	ds_read2_b32 v[24:25], v14 offset0:16 offset1:24
	ds_read2_b32 v[26:27], v14 offset0:82 offset1:90
	ds_read2_b32 v[28:29], v14 offset0:115 offset1:123
	ds_read2_b32 v[30:31], v14 offset0:148 offset1:156
	ds_read2_b32 v[32:33], v14 offset0:181 offset1:189
	ds_read2_b32 v[36:37], v14 offset0:214 offset1:222
	ds_read2_b32 v[38:39], v14 offset0:247 offset1:255
	v_lshl_add_u64 v[40:41], v[40:41], 0, v[12:13]
	s_waitcnt lgkmcnt(6)
	v_cvt_pk_bf16_f32 v18, v24, v22
	s_waitcnt lgkmcnt(4)
	v_cvt_pk_bf16_f32 v19, v26, v28
	s_waitcnt lgkmcnt(2)
	v_cvt_pk_bf16_f32 v20, v30, v32
	s_waitcnt lgkmcnt(0)
	v_cvt_pk_bf16_f32 v21, v36, v38
	global_store_dwordx4 v[40:41], v[18:21], off
	s_nop 1
	v_cvt_pk_bf16_f32 v18, v25, v23
	v_lshl_add_u64 v[22:23], s[4:5], 0, v[10:11]
	v_lshl_add_u64 v[22:23], v[22:23], 0, s[0:1]
	v_cvt_pk_bf16_f32 v19, v27, v29
	v_cvt_pk_bf16_f32 v20, v31, v33
	v_cvt_pk_bf16_f32 v21, v37, v39
	v_lshl_add_u64 v[22:23], v[22:23], 0, v[12:13]
	global_store_dwordx4 v[22:23], v[18:21], off
	s_waitcnt lgkmcnt(0)
	v_readlane_b32 s0, v253, 62
	s_add_i32 s24, s24, s0
	s_cmp_lt_i32 s24, s25
	s_cbranch_scc0 .LBB0_797

.LBB0_1345:
	v_bfe_u32 v12, v1, 5, 1
	s_lshl_b32 s0, s18, 14
	v_add_u32_e32 v2, s1, v12
	s_add_i32 s11, s0, 0
	v_mad_i64_i32 v[2:3], s[0:1], s10, v2, 0
	v_lshl_add_u64 v[2:3], v[2:3], 2, s[4:5]
	s_ashr_i32 s3, s2, 31
	v_and_b32_e32 v22, 31, v1
	v_lshl_add_u64 v[2:3], s[2:3], 2, v[2:3]
	v_lshlrev_b32_e32 v34, 2, v22
	s_mov_b32 s0, 0
	v_lshl_add_u64 v[2:3], v[2:3], 0, v[34:35]
	s_lshl_b32 s2, s10, 3
	s_mov_b32 s1, 1
	s_mov_b32 s3, s0
	global_load_dword v14, v[2:3], off nt
	v_lshl_add_u64 v[2:3], v[2:3], 0, s[2:3]
	global_load_dword v15, v[2:3], off nt
	v_lshl_add_u64 v[2:3], v[2:3], 0, s[2:3]
	global_load_dword v16, v[2:3], off nt
	v_lshl_add_u64 v[2:3], v[2:3], 0, s[2:3]
	global_load_dword v17, v[2:3], off nt
	v_lshl_add_u64 v[2:3], v[2:3], 0, s[2:3]
	global_load_dword v18, v[2:3], off nt
	v_lshl_add_u64 v[2:3], v[2:3], 0, s[2:3]
	global_load_dword v19, v[2:3], off nt
	v_lshl_add_u64 v[2:3], v[2:3], 0, s[2:3]
	global_load_dword v20, v[2:3], off nt
	v_lshl_add_u64 v[2:3], v[2:3], 0, s[2:3]
	global_load_dword v23, v[2:3], off nt
	v_lshl_add_u64 v[2:3], v[2:3], 0, s[2:3]
	global_load_dword v24, v[2:3], off nt
	v_lshl_add_u64 v[2:3], v[2:3], 0, s[2:3]
	global_load_dword v26, v[2:3], off nt
	v_lshl_add_u64 v[2:3], v[2:3], 0, s[2:3]
	global_load_dword v27, v[2:3], off nt
	v_lshl_add_u64 v[2:3], v[2:3], 0, s[2:3]
	global_load_dword v28, v[2:3], off nt
	v_lshl_add_u64 v[2:3], v[2:3], 0, s[2:3]
	global_load_dword v30, v[2:3], off nt
	v_lshl_add_u64 v[2:3], v[2:3], 0, s[2:3]
	global_load_dword v31, v[2:3], off nt
	v_lshl_add_u64 v[2:3], v[2:3], 0, s[2:3]
	global_load_dword v32, v[2:3], off nt
	v_lshl_add_u64 v[2:3], v[2:3], 0, s[2:3]
	global_load_dword v36, v[2:3], off nt
	v_lshl_add_u64 v[2:3], v[2:3], 0, s[2:3]
	global_load_dword v37, v[2:3], off nt
	v_lshl_add_u64 v[2:3], v[2:3], 0, s[2:3]
	global_load_dword v38, v[2:3], off nt
	v_lshl_add_u64 v[2:3], v[2:3], 0, s[2:3]
	global_load_dword v39, v[2:3], off nt
	v_lshl_add_u64 v[2:3], v[2:3], 0, s[2:3]
	global_load_dword v41, v[2:3], off nt
	v_lshl_add_u64 v[2:3], v[2:3], 0, s[2:3]
	global_load_dword v42, v[2:3], off nt
	v_lshl_add_u64 v[2:3], v[2:3], 0, s[2:3]
	global_load_dword v44, v[2:3], off nt
	v_lshl_add_u64 v[2:3], v[2:3], 0, s[2:3]
	global_load_dword v45, v[2:3], off nt
	v_lshl_add_u64 v[2:3], v[2:3], 0, s[2:3]
	global_load_dword v46, v[2:3], off nt
	v_lshl_add_u64 v[2:3], v[2:3], 0, s[2:3]
	global_load_dword v47, v[2:3], off nt
	v_lshl_add_u64 v[2:3], v[2:3], 0, s[2:3]
	global_load_dword v48, v[2:3], off nt
	v_lshl_add_u64 v[2:3], v[2:3], 0, s[2:3]
	global_load_dword v49, v[2:3], off nt
	v_lshl_add_u64 v[2:3], v[2:3], 0, s[2:3]
	global_load_dword v50, v[2:3], off nt
	v_lshl_add_u64 v[2:3], v[2:3], 0, s[2:3]
	global_load_dword v51, v[2:3], off nt
	v_lshl_add_u64 v[2:3], v[2:3], 0, s[2:3]
	global_load_dword v52, v[2:3], off nt
	v_lshl_add_u64 v[2:3], v[2:3], 0, s[2:3]
	global_load_dword v53, v[2:3], off nt
	v_lshl_add_u64 v[2:3], v[2:3], 0, s[2:3]
	global_load_dword v54, v[2:3], off nt
	v_readlane_b32 s0, v255, 37
	v_readlane_b32 s1, v255, 38
	v_readlane_b32 s36, v252, 48
	s_lshl_b64 s[2:3], s[0:1], 15
	s_lshl_b64 s[4:5], s[0:1], 16
	v_readlane_b32 s40, v252, 52
	v_readlane_b32 s41, v252, 53
	s_add_u32 s27, s40, s6
	v_bfe_u32 v4, v1, 3, 3
	v_lshlrev_b32_e32 v1, 3, v1
	s_addc_u32 s28, s41, s7
	v_and_b32_e32 v2, 56, v1
	v_readlane_b32 s37, v252, 49
	v_readlane_b32 s38, v252, 50
	v_readlane_b32 s39, v252, 51
	v_add_u32_e32 v13, s11, v34
	v_mul_u32_u24_e32 v21, 0x84, v12
	s_add_u32 s29, s36, s8
	v_mul_u32_u24_e32 v1, 0x84, v2
	v_lshlrev_b32_e32 v5, 2, v4
	v_lshlrev_b32_e32 v4, 10, v4
	s_addc_u32 s35, s37, s9
	v_mov_b32_e32 v3, v35
	v_add3_u32 v1, s11, v1, v5
	v_mov_b32_e32 v5, v35
	v_or_b32_e32 v6, 0x2000, v4
	v_mov_b32_e32 v7, v35
	v_or_b32_e32 v8, 0x4000, v4
	v_mov_b32_e32 v9, v35
	v_or_b32_e32 v10, 0x6000, v4
	v_mov_b32_e32 v11, v35
	s_lshl_b32 s36, s26, 5
	s_lshl_b32 s37, s44, 5
	s_lshl_b32 s38, s26, 1
	s_lshl_b32 s39, s44, 1
	v_lshlrev_b32_e32 v34, 2, v22
	v_add_u32_e32 v13, v13, v21
	v_readlane_b32 s42, v252, 54
	v_readlane_b32 s43, v252, 55
	s_branch .LBB0_1347

.LBB0_1356:
	v_add_u32_e32 v21, s1, v12
	v_mad_i64_i32 v[56:57], s[0:1], s24, v21, 0
	v_lshl_add_u64 v[56:57], v[56:57], 2, s[22:23]
	s_ashr_i32 s19, s18, 31
	v_lshl_add_u64 v[56:57], s[18:19], 2, v[56:57]
	s_mov_b32 s0, 0
	v_lshl_add_u64 v[56:57], v[56:57], 0, v[34:35]
	s_lshl_b32 s18, s24, 3
	s_mov_b32 s1, 1
	s_mov_b32 s19, s0
	global_load_dword v21, v[56:57], off nt
	v_lshl_add_u64 v[56:57], v[56:57], 0, s[18:19]
	global_load_dword v22, v[56:57], off nt
	v_lshl_add_u64 v[56:57], v[56:57], 0, s[18:19]
	global_load_dword v25, v[56:57], off nt
	v_lshl_add_u64 v[56:57], v[56:57], 0, s[18:19]
	global_load_dword v29, v[56:57], off nt
	v_lshl_add_u64 v[56:57], v[56:57], 0, s[18:19]
	global_load_dword v33, v[56:57], off nt
	v_lshl_add_u64 v[56:57], v[56:57], 0, s[18:19]
	global_load_dword v40, v[56:57], off nt
	v_lshl_add_u64 v[56:57], v[56:57], 0, s[18:19]
	global_load_dword v43, v[56:57], off nt
	v_lshl_add_u64 v[56:57], v[56:57], 0, s[18:19]
	v_lshl_add_u64 v[58:59], v[56:57], 0, s[18:19]
	global_load_dword v55, v[56:57], off nt
	s_nop 0
	global_load_dword v56, v[58:59], off nt
	v_lshl_add_u64 v[58:59], v[58:59], 0, s[18:19]
	v_lshl_add_u64 v[60:61], v[58:59], 0, s[18:19]
	global_load_dword v57, v[58:59], off nt
	s_nop 0
	global_load_dword v58, v[60:61], off nt
	v_lshl_add_u64 v[60:61], v[60:61], 0, s[18:19]
	v_lshl_add_u64 v[62:63], v[60:61], 0, s[18:19]
	global_load_dword v59, v[60:61], off nt
	s_nop 0
	global_load_dword v60, v[62:63], off nt
	v_lshl_add_u64 v[62:63], v[62:63], 0, s[18:19]
	v_lshl_add_u64 v[64:65], v[62:63], 0, s[18:19]
	global_load_dword v61, v[62:63], off nt
	s_nop 0
	global_load_dword v62, v[64:65], off nt
	v_lshl_add_u64 v[64:65], v[64:65], 0, s[18:19]
	v_lshl_add_u64 v[66:67], v[64:65], 0, s[18:19]
	global_load_dword v63, v[64:65], off nt
	s_nop 0
	global_load_dword v64, v[66:67], off nt
	v_lshl_add_u64 v[66:67], v[66:67], 0, s[18:19]
	v_lshl_add_u64 v[68:69], v[66:67], 0, s[18:19]
	global_load_dword v65, v[66:67], off nt
	s_nop 0
	global_load_dword v66, v[68:69], off nt
	v_lshl_add_u64 v[68:69], v[68:69], 0, s[18:19]
	v_lshl_add_u64 v[70:71], v[68:69], 0, s[18:19]
	global_load_dword v67, v[68:69], off nt
	s_nop 0
	global_load_dword v68, v[70:71], off nt
	v_lshl_add_u64 v[70:71], v[70:71], 0, s[18:19]
	v_lshl_add_u64 v[72:73], v[70:71], 0, s[18:19]
	global_load_dword v69, v[70:71], off nt
	s_nop 0
	global_load_dword v70, v[72:73], off nt
	v_lshl_add_u64 v[72:73], v[72:73], 0, s[18:19]
	v_lshl_add_u64 v[74:75], v[72:73], 0, s[18:19]
	global_load_dword v71, v[72:73], off nt
	s_nop 0
	global_load_dword v72, v[74:75], off nt
	v_lshl_add_u64 v[74:75], v[74:75], 0, s[18:19]
	v_lshl_add_u64 v[76:77], v[74:75], 0, s[18:19]
	global_load_dword v73, v[74:75], off nt
	s_nop 0
	global_load_dword v74, v[76:77], off nt
	v_lshl_add_u64 v[76:77], v[76:77], 0, s[18:19]
	v_lshl_add_u64 v[78:79], v[76:77], 0, s[18:19]
	global_load_dword v75, v[76:77], off nt
	s_nop 0
	global_load_dword v76, v[78:79], off nt
	v_lshl_add_u64 v[78:79], v[78:79], 0, s[18:19]
	v_lshl_add_u64 v[80:81], v[78:79], 0, s[18:19]
	global_load_dword v77, v[78:79], off nt
	s_nop 0
	global_load_dword v78, v[80:81], off nt
	v_lshl_add_u64 v[80:81], v[80:81], 0, s[18:19]
	global_load_dword v79, v[80:81], off nt
